# top-k radix-select loop counts with compare masks + scalar popcounts (s_bcnt1) instead of per-lane adds and a DPP wave reduction
# baseline (speedup 1.0000x reference)
.LBB0_790:
	s_lshl_b32 s0, 1, s3
	v_or_b32_e32 v35, s0, v45
	s_waitcnt vmcnt(0)
	s_mov_b32 s5, 0
	v_cmp_ge_u32_e64 s[6:7], v31, v35
	v_cmp_ge_u32_e64 s[8:9], v30, v35
	v_cmp_ge_u32_e64 s[10:11], v32, v35
	v_cmp_ge_u32_e64 s[12:13], v33, v35
	v_cmp_ge_u32_e64 s[14:15], v26, v35
	v_cmp_ge_u32_e64 s[16:17], v27, v35
	s_bcnt1_i32_b64 s0, s[6:7]
	s_add_i32 s5, s5, s0
	v_cmp_ge_u32_e64 s[6:7], v28, v35
	s_bcnt1_i32_b64 s0, s[8:9]
	s_add_i32 s5, s5, s0
	v_cmp_ge_u32_e64 s[8:9], v29, v35
	s_bcnt1_i32_b64 s0, s[10:11]
	s_add_i32 s5, s5, s0
	v_cmp_ge_u32_e64 s[10:11], v22, v35
	s_bcnt1_i32_b64 s0, s[12:13]
	s_add_i32 s5, s5, s0
	v_cmp_ge_u32_e64 s[12:13], v23, v35
	s_bcnt1_i32_b64 s0, s[14:15]
	s_add_i32 s5, s5, s0
	v_cmp_ge_u32_e64 s[14:15], v24, v35
	s_bcnt1_i32_b64 s0, s[16:17]
	s_add_i32 s5, s5, s0
	v_cmp_ge_u32_e64 s[16:17], v25, v35
	s_bcnt1_i32_b64 s0, s[6:7]
	s_add_i32 s5, s5, s0
	v_cmp_ge_u32_e64 s[6:7], v18, v35
	s_bcnt1_i32_b64 s0, s[8:9]
	s_add_i32 s5, s5, s0
	v_cmp_ge_u32_e64 s[8:9], v19, v35
	s_bcnt1_i32_b64 s0, s[10:11]
	s_add_i32 s5, s5, s0
	v_cmp_ge_u32_e64 s[10:11], v20, v35
	s_bcnt1_i32_b64 s0, s[12:13]
	s_add_i32 s5, s5, s0
	v_cmp_ge_u32_e64 s[12:13], v21, v35
	s_bcnt1_i32_b64 s0, s[14:15]
	s_add_i32 s5, s5, s0
	v_cmp_ge_u32_e64 s[14:15], v14, v35
	s_bcnt1_i32_b64 s0, s[16:17]
	s_add_i32 s5, s5, s0
	v_cmp_ge_u32_e64 s[16:17], v15, v35
	s_bcnt1_i32_b64 s0, s[6:7]
	s_add_i32 s5, s5, s0
	v_cmp_ge_u32_e64 s[6:7], v16, v35
	s_bcnt1_i32_b64 s0, s[8:9]
	s_add_i32 s5, s5, s0
	v_cmp_ge_u32_e64 s[8:9], v17, v35
	s_bcnt1_i32_b64 s0, s[10:11]
	s_add_i32 s5, s5, s0
	v_cmp_ge_u32_e64 s[10:11], v10, v35
	s_bcnt1_i32_b64 s0, s[12:13]
	s_add_i32 s5, s5, s0
	v_cmp_ge_u32_e64 s[12:13], v11, v35
	s_bcnt1_i32_b64 s0, s[14:15]
	s_add_i32 s5, s5, s0
	v_cmp_ge_u32_e64 s[14:15], v12, v35
	s_bcnt1_i32_b64 s0, s[16:17]
	s_add_i32 s5, s5, s0
	v_cmp_ge_u32_e64 s[16:17], v13, v35
	s_bcnt1_i32_b64 s0, s[6:7]
	s_add_i32 s5, s5, s0
	v_cmp_ge_u32_e64 s[6:7], v6, v35
	s_bcnt1_i32_b64 s0, s[8:9]
	s_add_i32 s5, s5, s0
	v_cmp_ge_u32_e64 s[8:9], v7, v35
	s_bcnt1_i32_b64 s0, s[10:11]
	s_add_i32 s5, s5, s0
	v_cmp_ge_u32_e64 s[10:11], v8, v35
	s_bcnt1_i32_b64 s0, s[12:13]
	s_add_i32 s5, s5, s0
	v_cmp_ge_u32_e64 s[12:13], v9, v35
	s_bcnt1_i32_b64 s0, s[14:15]
	s_add_i32 s5, s5, s0
	v_cmp_ge_u32_e64 s[14:15], v2, v35
	s_bcnt1_i32_b64 s0, s[16:17]
	s_add_i32 s5, s5, s0
	v_cmp_ge_u32_e64 s[16:17], v3, v35
	s_bcnt1_i32_b64 s0, s[6:7]
	s_add_i32 s5, s5, s0
	v_cmp_ge_u32_e64 s[6:7], v4, v35
	s_bcnt1_i32_b64 s0, s[8:9]
	s_add_i32 s5, s5, s0
	v_cmp_ge_u32_e64 s[8:9], v5, v35
	s_nop 1
	s_bcnt1_i32_b64 s0, s[10:11]
	s_add_i32 s5, s5, s0
	s_bcnt1_i32_b64 s0, s[12:13]
	s_add_i32 s5, s5, s0
	s_bcnt1_i32_b64 s0, s[14:15]
	s_add_i32 s5, s5, s0
	s_bcnt1_i32_b64 s0, s[16:17]
	s_add_i32 s5, s5, s0
	s_bcnt1_i32_b64 s0, s[6:7]
	s_add_i32 s5, s5, s0
	s_bcnt1_i32_b64 s0, s[8:9]
	s_add_i32 s5, s5, s0
	s_and_b32 s0, s2, 8
	s_lshl_b32 s0, s0, 2
	s_add_i32 s4, s0, 0
	v_mov_b32_e32 v36, s5
	s_and_saveexec_b64 s[0:1], vcc
	s_cbranch_execz .LBB0_789
	v_readlane_b32 s5, v254, 26
	s_add_i32 s5, s4, s5
	s_nop 0
	v_mov_b32_e32 v37, s5
	ds_write_b32 v37, v36
	s_branch .LBB0_789
